# gather at 4 waves per SIMD (VGPR alloc 128) and natural tile order, otherwise as previous
# speedup vs baseline: 1.0405x; 1.0172x over previous
_Z8k_gatherPK15HIP_vector_typeIiLj2EEPKjPKDv8_DF16_S7_PKfPf:
	s_lshr_b32 s3, s2, 3
	s_mul_hi_u32 s50, s3, 0xd1b71759
	s_lshr_b32 s50, s50, 10
	s_mulk_i32 s50, 0x4e2
	s_load_dwordx4 s[4:7], s[0:1], 0x0
	s_load_dwordx4 s[8:11], s[0:1], 0x10
	s_load_dwordx4 s[12:15], s[0:1], 0x20
	s_sub_i32 s3, s3, s50
	s_lshl_b32 s3, s3, 5
	s_and_b32 s51, s2, 7
	s_and_b32 s52, s2, 1
	s_lshr_b32 s53, s51, 1
	s_mul_i32 s53, s53, 0x9c40
	s_add_i32 s53, s53, s3
	v_and_b32_e32 v57, 7, v0
	v_lshrrev_b32_e32 v58, 3, v0
	v_lshlrev_b32_e32 v52, 4, v57
	v_add_u32_e32 v59, s3, v58
	v_add_u32_e32 v62, s53, v58
	v_lshlrev_b32_e32 v59, 3, v59
	v_lshl_add_u32 v63, v62, 8, v52
	v_lshl_add_u32 v54, v62, 9, v52
	s_mul_i32 s54, s51, 0x4e2000
	s_lshl_b32 s55, s52, 7
	s_lshl_b32 s56, s52, 8
	s_waitcnt lgkmcnt(0)
	global_load_dwordx2 v[60:61], v59, s[4:5]
	s_add_u32 s10, s10, s55
	s_addc_u32 s11, s11, 0
	global_load_dwordx4 v[8:11], v63, s[10:11] nt
	s_add_u32 s12, s12, s56
	s_addc_u32 s13, s13, 0
	global_load_dwordx4 v[4:7], v52, s[12:13]
	global_load_dwordx4 v[0:3], v52, s[12:13] offset:128
	s_add_u32 s14, s14, s56
	s_addc_u32 s15, s15, 0
	s_add_u32 s8, s8, s54
	s_addc_u32 s9, s9, 0
	s_mov_b32 s48, 0xffff
	v_mov_b32_e32 v56, 1.0
	s_waitcnt vmcnt(3)
	v_add_lshl_u32 v51, v60, v57, 2
	v_mov_b32_e32 v50, v61
	v_cmp_gt_i32_e32 vcc, v61, v57
	s_mov_b64 exec, vcc
	global_load_dword v49, v51, s[6:7]
	s_mov_b64 exec, -1
	s_waitcnt vmcnt(1)
	v_fma_mix_f32 v4, v8, v56, v4 op_sel_hi:[1,0,0]
	v_fma_mix_f32 v5, v8, v56, v5 op_sel:[1,0,0] op_sel_hi:[1,0,0]
	v_fma_mix_f32 v6, v9, v56, v6 op_sel_hi:[1,0,0]
	v_fma_mix_f32 v7, v9, v56, v7 op_sel:[1,0,0] op_sel_hi:[1,0,0]
	v_fma_mix_f32 v0, v10, v56, v0 op_sel_hi:[1,0,0]
	v_fma_mix_f32 v1, v10, v56, v1 op_sel:[1,0,0] op_sel_hi:[1,0,0]
	v_fma_mix_f32 v2, v11, v56, v2 op_sel_hi:[1,0,0]
	v_fma_mix_f32 v3, v11, v56, v3 op_sel:[1,0,0] op_sel_hi:[1,0,0]
	s_mov_b64 exec, -1
	s_waitcnt vmcnt(0)
	v_bfi_b32 v55, s48, v49, v48
	v_mov_b32_e32 v48, v49
	ds_swizzle_b32 v40, v55 offset:swizzle(BROADCAST,8,0)
	ds_swizzle_b32 v41, v55 offset:swizzle(BROADCAST,8,1)
	ds_swizzle_b32 v42, v55 offset:swizzle(BROADCAST,8,2)
	ds_swizzle_b32 v43, v55 offset:swizzle(BROADCAST,8,3)
	ds_swizzle_b32 v44, v55 offset:swizzle(BROADCAST,8,4)
	ds_swizzle_b32 v45, v55 offset:swizzle(BROADCAST,8,5)
	ds_swizzle_b32 v46, v55 offset:swizzle(BROADCAST,8,6)
	ds_swizzle_b32 v47, v55 offset:swizzle(BROADCAST,8,7)
	v_cmp_gt_i32_e64 s[32:33], v50, 0
	v_cmp_gt_i32_e64 s[34:35], v50, 1
	v_cmp_gt_i32_e64 s[36:37], v50, 2
	v_cmp_gt_i32_e64 s[38:39], v50, 3
	v_cmp_gt_i32_e64 s[40:41], v50, 4
	v_cmp_gt_i32_e64 s[42:43], v50, 5
	v_cmp_gt_i32_e64 s[44:45], v50, 6
	v_cmp_gt_i32_e64 s[46:47], v50, 7
	v_add_u32_e32 v50, -8, v50
	s_cmp_eq_u64 s[32:33], 0
	s_cbranch_scc1 .Lg_final
	v_cmp_gt_i32_e32 vcc, v50, v57
	v_add_u32_e32 v51, 32, v51
	s_mov_b64 exec, vcc
	global_load_dword v49, v51, s[6:7]
	s_waitcnt lgkmcnt(7)
	s_mov_b64 exec, s[32:33]
	v_and_b32_e32 v53, 0xffff, v40
	v_lshl_add_u32 v53, v53, 7, v52
	global_load_dwordx4 v[8:11], v53, s[8:9]
	s_waitcnt lgkmcnt(6)
	s_mov_b64 exec, s[34:35]
	v_and_b32_e32 v53, 0xffff, v41
	v_lshl_add_u32 v53, v53, 7, v52
	global_load_dwordx4 v[12:15], v53, s[8:9]
	s_waitcnt lgkmcnt(5)
	s_mov_b64 exec, s[36:37]
	v_and_b32_e32 v53, 0xffff, v42
	v_lshl_add_u32 v53, v53, 7, v52
	global_load_dwordx4 v[16:19], v53, s[8:9]
	s_waitcnt lgkmcnt(4)
	s_mov_b64 exec, s[38:39]
	v_and_b32_e32 v53, 0xffff, v43
	v_lshl_add_u32 v53, v53, 7, v52
	global_load_dwordx4 v[20:23], v53, s[8:9]
	s_waitcnt lgkmcnt(3)
	s_mov_b64 exec, s[40:41]
	v_and_b32_e32 v53, 0xffff, v44
	v_lshl_add_u32 v53, v53, 7, v52
	global_load_dwordx4 v[24:27], v53, s[8:9]
	s_waitcnt lgkmcnt(2)
	s_mov_b64 exec, s[42:43]
	v_and_b32_e32 v53, 0xffff, v45
	v_lshl_add_u32 v53, v53, 7, v52
	global_load_dwordx4 v[28:31], v53, s[8:9]
	s_waitcnt lgkmcnt(1)
	s_mov_b64 exec, s[44:45]
	v_and_b32_e32 v53, 0xffff, v46
	v_lshl_add_u32 v53, v53, 7, v52
	global_load_dwordx4 v[32:35], v53, s[8:9]
	s_waitcnt lgkmcnt(0)
	s_mov_b64 exec, s[46:47]
	v_and_b32_e32 v53, 0xffff, v47
	v_lshl_add_u32 v53, v53, 7, v52
	global_load_dwordx4 v[36:39], v53, s[8:9]
	s_mov_b64 s[16:17], s[32:33]
	s_mov_b64 s[18:19], s[34:35]
	s_mov_b64 s[20:21], s[36:37]
	s_mov_b64 s[22:23], s[38:39]
	s_mov_b64 s[24:25], s[40:41]
	s_mov_b64 s[26:27], s[42:43]
	s_mov_b64 s[28:29], s[44:45]
	s_mov_b64 s[30:31], s[46:47]

	.amdhsa_kernel _Z8k_gatherPK15HIP_vector_typeIiLj2EEPKjPKDv8_DF16_S7_PKfPf
		.amdhsa_group_segment_fixed_size 0
		.amdhsa_private_segment_fixed_size 0
		.amdhsa_kernarg_size 48
		.amdhsa_user_sgpr_count 2
		.amdhsa_user_sgpr_dispatch_ptr 0
		.amdhsa_user_sgpr_queue_ptr 0
		.amdhsa_user_sgpr_kernarg_segment_ptr 1
		.amdhsa_user_sgpr_dispatch_id 0
		.amdhsa_user_sgpr_kernarg_preload_length 0
		.amdhsa_user_sgpr_kernarg_preload_offset 0
		.amdhsa_user_sgpr_private_segment_size 0
		.amdhsa_uses_dynamic_stack 0
		.amdhsa_enable_private_segment 0
		.amdhsa_system_sgpr_workgroup_id_x 1
		.amdhsa_system_sgpr_workgroup_id_y 0
		.amdhsa_system_sgpr_workgroup_id_z 0
		.amdhsa_system_sgpr_workgroup_info 0
		.amdhsa_system_vgpr_workitem_id 0
		.amdhsa_next_free_vgpr 128
		.amdhsa_next_free_sgpr 57
		.amdhsa_accum_offset 128
		.amdhsa_reserve_vcc 1
		.amdhsa_float_round_mode_32 0
		.amdhsa_float_round_mode_16_64 0
		.amdhsa_float_denorm_mode_32 3
		.amdhsa_float_denorm_mode_16_64 3
		.amdhsa_dx10_clamp 1
		.amdhsa_ieee_mode 1
		.amdhsa_fp16_overflow 0
		.amdhsa_tg_split 0
		.amdhsa_exception_fp_ieee_invalid_op 0
		.amdhsa_exception_fp_denorm_src 0
		.amdhsa_exception_fp_ieee_div_zero 0
		.amdhsa_exception_fp_ieee_overflow 0
		.amdhsa_exception_fp_ieee_underflow 0
		.amdhsa_exception_fp_ieee_inexact 0
		.amdhsa_exception_int_div_zero 0
	.end_amdhsa_kernel

amdhsa.kernels:
  - .agpr_count:     0
    .args:
      - .actual_access:  read_only
        .address_space:  global
        .offset:         0
        .size:           8
        .value_kind:     global_buffer
      - .actual_access:  read_only
        .address_space:  global
        .offset:         8
        .size:           8
        .value_kind:     global_buffer
      - .actual_access:  read_only
        .address_space:  global
        .offset:         16
        .size:           8
        .value_kind:     global_buffer
      - .actual_access:  write_only
        .address_space:  global
        .offset:         24
        .size:           8
        .value_kind:     global_buffer
      - .actual_access:  write_only
        .address_space:  global
        .offset:         32
        .size:           8
        .value_kind:     global_buffer
      - .actual_access:  read_only
        .address_space:  global
        .offset:         40
        .size:           8
        .value_kind:     global_buffer
      - .actual_access:  read_only
        .address_space:  global
        .offset:         48
        .size:           8
        .value_kind:     global_buffer
      - .actual_access:  write_only
        .address_space:  global
        .offset:         56
        .size:           8
        .value_kind:     global_buffer
      - .actual_access:  read_only
        .address_space:  global
        .offset:         64
        .size:           8
        .value_kind:     global_buffer
    .group_segment_fixed_size: 27200
    .kernarg_segment_align: 8
    .kernarg_segment_size: 72
    .language:       OpenCL C
    .language_version:
      - 2
      - 0
    .max_flat_workgroup_size: 1024
    .name:           _Z6k_partPKiS0_PKfP15HIP_vector_typeIiLj2EEPiS2_S2_PDv8_DF16_S6_
    .private_segment_fixed_size: 0
    .sgpr_count:     30
    .sgpr_spill_count: 0
    .symbol:         _Z6k_partPKiS0_PKfP15HIP_vector_typeIiLj2EEPiS2_S2_PDv8_DF16_S6_.kd
    .uniform_work_group_size: 1
    .uses_dynamic_stack: false
    .vgpr_count:     30
    .vgpr_spill_count: 0
    .wavefront_size: 64
  - .agpr_count:     0
    .args:
      - .actual_access:  read_only
        .address_space:  global
        .offset:         0
        .size:           8
        .value_kind:     global_buffer
      - .actual_access:  read_only
        .address_space:  global
        .offset:         8
        .size:           8
        .value_kind:     global_buffer
      - .actual_access:  write_only
        .address_space:  global
        .offset:         16
        .size:           8
        .value_kind:     global_buffer
      - .actual_access:  write_only
        .address_space:  global
        .offset:         24
        .size:           8
        .value_kind:     global_buffer
      - .actual_access:  read_only
        .address_space:  global
        .offset:         32
        .size:           8
        .value_kind:     global_buffer
      - .actual_access:  read_only
        .address_space:  global
        .offset:         40
        .size:           8
        .value_kind:     global_buffer
      - .actual_access:  read_only
        .address_space:  global
        .offset:         48
        .size:           8
        .value_kind:     global_buffer
      - .actual_access:  write_only
        .address_space:  global
        .offset:         56
        .size:           8
        .value_kind:     global_buffer
      - .actual_access:  write_only
        .address_space:  global
        .offset:         64
        .size:           8
        .value_kind:     global_buffer
    .group_segment_fixed_size: 51200
    .kernarg_segment_align: 8
    .kernarg_segment_size: 72
    .language:       OpenCL C
    .language_version:
      - 2
      - 0
    .max_flat_workgroup_size: 256
    .name:           _Z6k_gemmPKfPKDv8_DF16_PDF16_S4_PK15HIP_vector_typeIiLj2EEPKiPiPS6_Pj
    .private_segment_fixed_size: 0
    .sgpr_count:     44
    .sgpr_spill_count: 0
    .symbol:         _Z6k_gemmPKfPKDv8_DF16_PDF16_S4_PK15HIP_vector_typeIiLj2EEPKiPiPS6_Pj.kd
    .uniform_work_group_size: 1
    .uses_dynamic_stack: false
    .vgpr_count:     166
    .vgpr_spill_count: 0
    .wavefront_size: 64
  - .agpr_count:     0
    .args:
      - .actual_access:  read_only
        .address_space:  global
        .offset:         0
        .size:           8
        .value_kind:     global_buffer
      - .actual_access:  read_only
        .address_space:  global
        .offset:         8
        .size:           8
        .value_kind:     global_buffer
      - .actual_access:  read_only
        .address_space:  global
        .offset:         16
        .size:           8
        .value_kind:     global_buffer
      - .actual_access:  read_only
        .address_space:  global
        .offset:         24
        .size:           8
        .value_kind:     global_buffer
      - .actual_access:  read_only
        .address_space:  global
        .offset:         32
        .size:           8
        .value_kind:     global_buffer
      - .actual_access:  write_only
        .address_space:  global
        .offset:         40
        .size:           8
        .value_kind:     global_buffer
    .group_segment_fixed_size: 0
    .kernarg_segment_align: 8
    .kernarg_segment_size: 48
    .language:       OpenCL C
    .language_version:
      - 2
      - 0
    .max_flat_workgroup_size: 256
    .name:           _Z8k_gatherPK15HIP_vector_typeIiLj2EEPKjPKDv8_DF16_S7_PKfPf
    .private_segment_fixed_size: 0
    .sgpr_count:     63
    .sgpr_spill_count: 0
    .symbol:         _Z8k_gatherPK15HIP_vector_typeIiLj2EEPKjPKDv8_DF16_S7_PKfPf.kd
    .uniform_work_group_size: 1
    .uses_dynamic_stack: false
    .vgpr_count:     128
    .vgpr_spill_count: 0
    .wavefront_size: 64
